# plus: layer 1 projection phase, the 32 workgroups without a second tile convert the last 192 tile pairs (layer-1 down weights) in their idle slot
# speedup vs baseline: 1.0331x; 1.0088x over previous
; #define REP(k) _Pragma("unroll") for (int rep_ = 0; rep_ < 1 + (int)(((REP_MASK) >> (k)) & 1u); ++rep_)
; #define SEAM(k) do { if (IN(k) && IN((k) + 1)) xcd_barrier(bar); } while (0)
; __global__ void __launch_bounds__(512, 2) mk_fwd(Params p) {
;     ...
;         if (EN(4) && IN(pb + 1) && (!split || bx < MIX_GW)) REP(4) {
;             SchedProj S{H, (const char*)(p.ws + WS_WIN) + (size_t)l * NPROJ * 2048 * 2, (const char*)(p.ws + WS_WPQ) + (size_t)l * 512 * 2048 * 2, vG, bx};
;             EpiProj E{(bf16_t*)(p.ws + WS_PROJ), (bf16_t*)(p.ws + WS_PQT), (const float*)(p.ws + WS_ROPE), (const float*)(p.ws + WS_ROPE) + NT * 8};
;             pg8::gemm_phase<EpiProj, SchedProj>(lds, 2048, 2048, 2048, S, E);
;         }
;         if (split) { if (bx < MIX_GW && IN(pb + 1) && IN(pb + 2)) xcd_barrier(bar2); } else SEAM(pb + 1);
.LBB0_669:
	s_waitcnt vmcnt(0)
	v_readlane_b32 s36, v255, 61
	s_movk_i32 s43, 0x4000
	s_mov_b32 s29, s94
	v_readlane_b32 s37, v255, 62
	s_barrier
	v_readlane_b32 s8, v250, 59
	v_readlane_b32 s9, v249, 28
	s_nop 3
	s_cmp_eq_u32 s8, 1
	s_cbranch_scc0 .LBB0_670
	s_cmpk_lt_u32 s9, 0xe0
	s_cbranch_scc1 .LBB0_670
	s_branch .Lcv_idle

; #define LAS __attribute__((address_space(3)))
; __device__ __forceinline__ int opaque_tid() { int t = threadIdx.x; asm volatile("" : "+v"(t)); return t; }
; #define REP(k) _Pragma("unroll") for (int rep_ = 0; rep_ < 1 + (int)(((REP_MASK) >> (k)) & 1u); ++rep_)
; #define SEAM(k) do { if (IN(k) && IN((k) + 1)) xcd_barrier(bar); } while (0)
; __device__ __forceinline__ void ph_weights(const Params& p, LAS unsigned char* lds, const int p0, const int p1, const int wi, const int wn) {
;     const int tid = opaque_tid();
;     LAS unsigned* l32 = (LAS unsigned*)lds;
;     LAS bf16_t* l16 = (LAS bf16_t*)lds;
;     TDesc dA0, dA1, dB0, dB1; f32x4 a0[8], a1[8], b0[8], b1[8];
;     ...
;     int pi = p0 + wi; bool hA, hB;
;     PW_LOAD(pi, dA0, dA1, a0, a1, hA);
;     PW_LOAD(pi + wn, dB0, dB1, b0, b1, hB);
; __global__ void __launch_bounds__(512, 2) mk_fwd(Params p) {
;     ...
;         if (EN(4) && IN(pb + 1) && (!split || bx < MIX_GW)) REP(4) {
;             SchedProj S{H, (const char*)(p.ws + WS_WIN) + (size_t)l * NPROJ * 2048 * 2, (const char*)(p.ws + WS_WPQ) + (size_t)l * 512 * 2048 * 2, vG, bx};
;             EpiProj E{(bf16_t*)(p.ws + WS_PROJ), (bf16_t*)(p.ws + WS_PQT), (const float*)(p.ws + WS_ROPE), (const float*)(p.ws + WS_ROPE) + NT * 8};
;             pg8::gemm_phase<EpiProj, SchedProj>(lds, 2048, 2048, 2048, S, E);
;         }
;         if (split) { if (bx < MIX_GW && IN(pb + 1) && IN(pb + 2)) xcd_barrier(bar2); } else SEAM(pb + 1);
.LBB0_779:
	v_readlane_b32 s0, v249, 28
	s_nop 3
	s_add_u32 s0, s0, 80
	s_movk_i32 s70, 96
	s_movk_i32 s71, 0x16b0
	s_mov_b32 s74, 0
	v_writelane_b32 v255, s29, 61
	s_branch .Lcv_common
.Lcv_late:
	v_readlane_b32 s0, v249, 28
	s_nop 3
	s_add_u32 s0, s0, 5680
	s_movk_i32 s70, 32
	s_movk_i32 s71, 0x1920
	s_mov_b32 s74, 0
	v_writelane_b32 v255, s29, 61
	s_branch .Lcv_common
.Lcv_idle:
	v_writelane_b32 v246, s14, 0
	v_writelane_b32 v246, s15, 1
	v_writelane_b32 v246, s20, 2
	v_writelane_b32 v246, s21, 3
	v_writelane_b32 v246, s29, 4
	v_writelane_b32 v246, s30, 5
	v_writelane_b32 v246, s31, 6
	v_writelane_b32 v246, s36, 7
	v_writelane_b32 v246, s37, 8
	v_writelane_b32 v246, s56, 9
	v_writelane_b32 v246, s57, 10
	v_writelane_b32 v246, s69, 11
	s_mov_b32 s74, 1
	s_waitcnt vmcnt(0) lgkmcnt(0)
	s_barrier
	v_readlane_b32 s0, v249, 28
	s_nop 3
	s_add_u32 s0, s0, 6464
	s_movk_i32 s70, 32
	s_movk_i32 s71, 0x1ae0
	s_branch .Lcv_common
.Lcv_tail:
	v_writelane_b32 v246, s14, 0
	v_writelane_b32 v246, s15, 1
	v_writelane_b32 v246, s20, 2
	v_writelane_b32 v246, s21, 3
	v_writelane_b32 v246, s29, 4
	v_writelane_b32 v246, s30, 5
	v_writelane_b32 v246, s31, 6
	v_writelane_b32 v246, s36, 7
	v_writelane_b32 v246, s37, 8
	v_writelane_b32 v246, s56, 9
	v_writelane_b32 v246, s57, 10
	v_writelane_b32 v246, s69, 11
	s_mov_b32 s74, 2
	s_waitcnt vmcnt(0) lgkmcnt(0)
	s_barrier
	v_readlane_b32 s0, v249, 28
	s_nop 3
	s_add_u32 s0, s0, 6432
	s_movk_i32 s70, 128
	s_movk_i32 s71, 0x1a20

; #define REP(k) _Pragma("unroll") for (int rep_ = 0; rep_ < 1 + (int)(((REP_MASK) >> (k)) & 1u); ++rep_)
; #define SEAM(k) do { if (IN(k) && IN((k) + 1)) xcd_barrier(bar); } while (0)
; __global__ void __launch_bounds__(512, 2) mk_fwd(Params p) {
;     ...
;         if (EN(4) && IN(pb + 1) && (!split || bx < MIX_GW)) REP(4) {
;             SchedProj S{H, (const char*)(p.ws + WS_WIN) + (size_t)l * NPROJ * 2048 * 2, (const char*)(p.ws + WS_WPQ) + (size_t)l * 512 * 2048 * 2, vG, bx};
;             EpiProj E{(bf16_t*)(p.ws + WS_PROJ), (bf16_t*)(p.ws + WS_PQT), (const float*)(p.ws + WS_ROPE), (const float*)(p.ws + WS_ROPE) + NT * 8};
;             pg8::gemm_phase<EpiProj, SchedProj>(lds, 2048, 2048, 2048, S, E);
;         }
;         if (split) { if (bx < MIX_GW && IN(pb + 1) && IN(pb + 2)) xcd_barrier(bar2); } else SEAM(pb + 1);
.Lcv_done:
	s_waitcnt vmcnt(0)
	s_cmp_eq_u32 s74, 0
	s_cbranch_scc1 .LBB0_902
	v_readlane_b32 s14, v246, 0
	v_readlane_b32 s15, v246, 1
	v_readlane_b32 s20, v246, 2
	v_readlane_b32 s21, v246, 3
	v_readlane_b32 s29, v246, 4
	v_readlane_b32 s30, v246, 5
	v_readlane_b32 s31, v246, 6
	v_readlane_b32 s36, v246, 7
	v_readlane_b32 s37, v246, 8
	v_readlane_b32 s56, v246, 9
	v_readlane_b32 s57, v246, 10
	v_readlane_b32 s69, v246, 11
	s_nop 3
	s_barrier
	s_cmp_eq_u32 s74, 1
	s_cbranch_scc1 .LBB0_670
	s_branch .Lcv_ret986
